# speedup vs baseline: 1.0125x; 1.0109x over previous
.LBB1_20:
	s_add_u32 s45, s12, 0x200000
	s_addc_u32 s46, s13, 0
	s_cmpk_lt_u32 s21, 0x100
	s_cselect_b64 s[22:23], -1, 0
	s_or_b64 s[26:27], s[16:17], s[22:23]
	s_and_b64 s[0:1], s[26:27], exec
	s_cselect_b32 s31, s13, s46
	s_cselect_b32 s34, s12, s45
	s_add_u32 s0, s12, 0x400000
	s_addc_u32 s1, s13, 0
	s_lshl_b32 s24, s9, 6
	s_ashr_i32 s25, s24, 31
	s_lshl_b64 s[24:25], s[24:25], 4
	s_add_u32 s34, s34, s24
	s_addc_u32 s35, s31, s25
	s_lshl_b32 s24, s42, 4
	s_and_b64 s[26:27], s[26:27], exec
	s_cselect_b32 s9, s46, s13
	s_cselect_b32 s25, s45, s12
	s_and_b64 s[26:27], exec, s[16:17]
	v_mul_u32_u24_e32 v20, 0x2aab, v0
	s_cselect_b32 s8, s8, s24
	v_lshrrev_b32_e32 v156, 16, v20
	s_add_i32 s4, s4, s8
	s_lshl_b32 s8, s3, 2
	v_mul_lo_u16_e32 v20, 6, v156
	s_and_b32 s47, s8, 12
	v_sub_u16_e32 v20, v0, v20
	s_or_b32 s4, s4, s47
	v_lshlrev_b32_e32 v20, 2, v20
	v_lshl_or_b32 v24, s4, 6, v199
	global_load_dword v176, v20, s[14:15]
	v_mov_b32_e32 v20, s25
	v_mov_b32_e32 v21, s9
	v_ashrrev_i32_e32 v25, 31, v24
	v_mov_b32_e32 v167, 0
	v_lshlrev_b32_e32 v166, 4, v199
	v_lshl_add_u64 v[20:21], v[24:25], 4, v[20:21]
	s_mov_b32 s5, 0
	v_lshl_add_u64 v[18:19], s[34:35], 0, v[166:167]
	global_load_dwordx4 v[146:149], v[20:21], off
	global_load_dwordx4 v[138:141], v[20:21], off offset:1024
	global_load_dwordx4 v[24:27], v166, s[34:35]
	s_lshl_b32 s4, s20, 4
	v_lshl_add_u64 v[18:19], v[18:19], 0, s[4:5]
	global_load_dwordx4 v[28:31], v[18:19], off
	global_load_dwordx4 v[150:153], v[20:21], off offset:2048
	global_load_dwordx4 v[142:145], v[20:21], off offset:3072
	s_lshl_b32 s9, s21, 4
	s_and_b32 s8, s21, 64
	s_and_b32 s9, s9, 0xfffff800
	s_or_b32 s8, s8, s9
	v_or_b32_e32 v34, s8, v199
	v_lshl_add_u64 v[32:33], v[18:19], 0, s[4:5]
	v_ashrrev_i32_e32 v35, 31, v34
	v_or_b32_e32 v38, 0x80, v34
	global_load_dwordx4 v[18:21], v[32:33], off
	v_lshl_add_u64 v[32:33], v[32:33], 0, s[4:5]
	v_lshl_add_u64 v[36:37], v[34:35], 4, s[0:1]
	v_ashrrev_i32_e32 v39, 31, v38
	global_load_dwordx4 v[62:65], v[32:33], off
	v_lshl_add_u64 v[38:39], v[38:39], 4, s[0:1]
	global_load_dwordx4 v[122:125], v[36:37], off
	global_load_dwordx4 v[98:101], v[38:39], off
	v_or_b32_e32 v36, 0x100, v34
	v_ashrrev_i32_e32 v37, 31, v36
	v_or_b32_e32 v38, 0x180, v34
	v_lshl_add_u64 v[36:37], v[36:37], 4, s[0:1]
	v_ashrrev_i32_e32 v39, 31, v38
	v_lshl_add_u64 v[38:39], v[38:39], 4, s[0:1]
	global_load_dwordx4 v[114:117], v[36:37], off
	global_load_dwordx4 v[86:89], v[38:39], off
	v_or_b32_e32 v36, 0x200, v34
	v_ashrrev_i32_e32 v37, 31, v36
	v_or_b32_e32 v38, 0x280, v34
	v_lshl_add_u64 v[36:37], v[36:37], 4, s[0:1]
	v_ashrrev_i32_e32 v39, 31, v38
	v_lshl_add_u64 v[38:39], v[38:39], 4, s[0:1]
	global_load_dwordx4 v[126:129], v[36:37], off
	global_load_dwordx4 v[90:93], v[38:39], off
	v_or_b32_e32 v36, 0x300, v34
	v_ashrrev_i32_e32 v37, 31, v36
	v_or_b32_e32 v38, 0x380, v34
	v_lshl_add_u64 v[36:37], v[36:37], 4, s[0:1]
	v_ashrrev_i32_e32 v39, 31, v38
	v_lshl_add_u64 v[38:39], v[38:39], 4, s[0:1]
	global_load_dwordx4 v[118:121], v[36:37], off
	global_load_dwordx4 v[78:81], v[38:39], off
	v_or_b32_e32 v36, 0x400, v34
	v_ashrrev_i32_e32 v37, 31, v36
	v_or_b32_e32 v38, 0x480, v34
	v_lshl_add_u64 v[36:37], v[36:37], 4, s[0:1]
	v_ashrrev_i32_e32 v39, 31, v38
	v_lshl_add_u64 v[38:39], v[38:39], 4, s[0:1]
	global_load_dwordx4 v[102:105], v[36:37], off
	global_load_dwordx4 v[74:77], v[38:39], off
	v_or_b32_e32 v36, 0x500, v34
	v_ashrrev_i32_e32 v37, 31, v36
	v_or_b32_e32 v38, 0x580, v34
	v_lshl_add_u64 v[36:37], v[36:37], 4, s[0:1]
	v_ashrrev_i32_e32 v39, 31, v38
	v_lshl_add_u64 v[38:39], v[38:39], 4, s[0:1]
	global_load_dwordx4 v[106:109], v[36:37], off
	global_load_dwordx4 v[82:85], v[38:39], off
	v_or_b32_e32 v36, 0x600, v34
	v_ashrrev_i32_e32 v37, 31, v36
	v_or_b32_e32 v38, 0x680, v34
	v_lshl_add_u64 v[36:37], v[36:37], 4, s[0:1]
	v_ashrrev_i32_e32 v39, 31, v38
	v_lshl_add_u64 v[38:39], v[38:39], 4, s[0:1]
	global_load_dwordx4 v[110:113], v[36:37], off
	global_load_dwordx4 v[94:97], v[38:39], off
	v_or_b32_e32 v36, 0x700, v34
	v_ashrrev_i32_e32 v37, 31, v36
	v_or_b32_e32 v34, 0x780, v34
	v_lshl_add_u64 v[36:37], v[36:37], 4, s[0:1]
	v_ashrrev_i32_e32 v35, 31, v34
	v_lshlrev_b32_e32 v23, 3, v199
	s_mulk_i32 s3, 0x840
	v_lshl_add_u64 v[34:35], v[34:35], 4, s[0:1]
	global_load_dwordx4 v[134:137], v[36:37], off
	global_load_dwordx4 v[130:133], v[34:35], off
	v_add_u32_e32 v189, s3, v23
	v_and_b32_e32 v157, 31, v0
	v_lshlrev_b32_e32 v22, 4, v22
	s_movk_i32 s0, 0x210
	v_mad_u32_u24 v179, v157, s0, v22
	s_waitcnt vmcnt(21)
	v_pk_add_f16 v36, v24, v146
	v_pk_add_f16 v37, v25, v147
	s_waitcnt vmcnt(20)
	v_pk_add_f16 v23, v28, v146
	v_pk_mul_f16 v34, v26, v148 clamp
	v_pk_mul_f16 v35, v27, v149 clamp
	v_pk_max_f16 v34, v36, v34
	v_pk_max_f16 v35, v37, v35
	v_pk_add_f16 v38, v29, v147
	v_pk_add_f16 v40, v25, v139
	v_pk_mul_f16 v36, v30, v148 clamp
	v_pk_mul_f16 v37, v31, v149 clamp
	v_pk_max_f16 v36, v23, v36
	v_pk_max_f16 v37, v38, v37
	v_pk_add_f16 v23, v24, v138
	s_nop 0
	v_pk_mul_f16 v38, v26, v140 clamp
	v_pk_mul_f16 v39, v27, v141 clamp
	v_pk_max_f16 v38, v23, v38
	v_pk_max_f16 v39, v40, v39
	v_pk_add_f16 v23, v28, v138
	ds_write2_b64 v189, v[34:35], v[38:39] offset1:66
	v_pk_add_f16 v38, v29, v139
	s_nop 0
	v_pk_mul_f16 v34, v30, v140 clamp
	v_pk_mul_f16 v35, v31, v141 clamp
	v_pk_max_f16 v34, v23, v34
	v_pk_max_f16 v35, v38, v35
	v_add_u32_e32 v23, 0x4000, v189
	ds_write2_b64 v23, v[36:37], v[34:35] offset0:64 offset1:130
	s_waitcnt vmcnt(19)
	v_pk_add_f16 v23, v24, v150
	v_pk_add_f16 v36, v25, v151
	v_pk_add_f16 v38, v29, v151
	v_pk_mul_f16 v34, v26, v152 clamp
	v_pk_mul_f16 v35, v27, v153 clamp
	v_pk_max_f16 v34, v23, v34
	v_pk_max_f16 v35, v36, v35
	v_pk_add_f16 v23, v28, v150
	s_nop 0
	v_pk_mul_f16 v36, v30, v152 clamp
	v_pk_mul_f16 v37, v31, v153 clamp
	v_pk_max_f16 v36, v23, v36
	v_pk_max_f16 v37, v38, v37
	s_waitcnt vmcnt(18)
	v_pk_add_f16 v23, v24, v142
	v_pk_add_f16 v38, v25, v143
	s_nop 0
	v_pk_mul_f16 v24, v26, v144 clamp
	v_pk_mul_f16 v25, v27, v145 clamp
	v_pk_max_f16 v24, v23, v24
	v_pk_max_f16 v25, v38, v25
	v_pk_add_f16 v23, v28, v142
	ds_write2_b64 v189, v[34:35], v[24:25] offset0:132 offset1:198
	v_pk_add_f16 v26, v29, v143
	s_nop 0
	v_pk_mul_f16 v24, v30, v144 clamp
	v_pk_mul_f16 v25, v31, v145 clamp
	v_pk_max_f16 v24, v23, v24
	v_pk_max_f16 v25, v26, v25
	v_add_u32_e32 v23, 0x4400, v189
	v_lshl_add_u64 v[30:31], v[32:33], 0, s[4:5]
	ds_write2_b64 v23, v[36:37], v[24:25] offset0:68 offset1:134
	s_waitcnt lgkmcnt(0)
	s_barrier
	global_load_dwordx4 v[158:161], v[30:31], off
	ds_read_b128 v[22:25], v179
	ds_read_b128 v[26:29], v179 offset:32
	ds_read_b128 v[46:49], v179 offset:64
	ds_read_b128 v[50:53], v179 offset:96
	ds_read_b128 v[54:57], v179 offset:128
	ds_read_b128 v[58:61], v179 offset:160
	v_lshl_add_u64 v[154:155], v[30:31], 0, s[4:5]
	s_waitcnt vmcnt(16) lgkmcnt(5)
	v_mfma_f32_32x32x16_f16 v[30:45], v[122:125], v[22:25], v[2:17]
	s_and_b64 vcc, exec, s[16:17]
	s_cbranch_vccnz .Lw2_keep
	v_mov_b32_dpp v70, v70 row_shl:8 row_mask:0xa bank_mask:0x3
	v_mov_b32_dpp v71, v71 row_shl:8 row_mask:0xa bank_mask:0x3
	v_mov_b32_dpp v72, v72 row_shl:8 row_mask:0xa bank_mask:0x3
	v_mov_b32_dpp v73, v73 row_shl:8 row_mask:0xa bank_mask:0x3
	v_mov_b32_dpp v66, v66 row_shl:8 row_mask:0xa bank_mask:0x3
	v_mov_b32_dpp v67, v67 row_shl:8 row_mask:0xa bank_mask:0x3
	v_mov_b32_dpp v68, v68 row_shl:8 row_mask:0xa bank_mask:0x3
	v_mov_b32_dpp v69, v69 row_shl:8 row_mask:0xa bank_mask:0x3
.Lw2_keep:
	ds_read_b128 v[162:165], v179 offset:192
	s_waitcnt vmcnt(15) lgkmcnt(5)
	v_mfma_f32_32x32x16_f16 v[30:45], v[98:101], v[26:29], v[30:45]
	ds_read_b128 v[22:25], v179 offset:224
	s_waitcnt vmcnt(14) lgkmcnt(5)
	v_mfma_f32_32x32x16_f16 v[30:45], v[114:117], v[46:49], v[30:45]
	ds_read_b128 v[26:29], v179 offset:256
	s_waitcnt vmcnt(13) lgkmcnt(5)
	v_mfma_f32_32x32x16_f16 v[30:45], v[86:89], v[50:53], v[30:45]
	ds_read_b128 v[46:49], v179 offset:288
	s_waitcnt vmcnt(12) lgkmcnt(5)
	v_mfma_f32_32x32x16_f16 v[30:45], v[126:129], v[54:57], v[30:45]
	ds_read_b128 v[50:53], v179 offset:320
	s_waitcnt vmcnt(11) lgkmcnt(5)
	v_mfma_f32_32x32x16_f16 v[30:45], v[90:93], v[58:61], v[30:45]
	ds_read_b128 v[54:57], v179 offset:352
	s_waitcnt vmcnt(10) lgkmcnt(5)
	v_mfma_f32_32x32x16_f16 v[30:45], v[118:121], v[162:165], v[30:45]
	ds_read_b128 v[58:61], v179 offset:384
	s_waitcnt vmcnt(9) lgkmcnt(5)
	v_mfma_f32_32x32x16_f16 v[30:45], v[78:81], v[22:25], v[30:45]
	ds_read_b128 v[162:165], v179 offset:416
	s_waitcnt vmcnt(8) lgkmcnt(5)
	v_mfma_f32_32x32x16_f16 v[30:45], v[102:105], v[26:29], v[30:45]
	ds_read_b128 v[22:25], v179 offset:448
	s_waitcnt vmcnt(7) lgkmcnt(5)
	v_mfma_f32_32x32x16_f16 v[30:45], v[74:77], v[46:49], v[30:45]
	ds_read_b128 v[26:29], v179 offset:480
	s_waitcnt vmcnt(6) lgkmcnt(5)
	v_mfma_f32_32x32x16_f16 v[30:45], v[106:109], v[50:53], v[30:45]
	s_waitcnt vmcnt(5) lgkmcnt(4)
	v_mfma_f32_32x32x16_f16 v[30:45], v[82:85], v[54:57], v[30:45]
	s_waitcnt vmcnt(4) lgkmcnt(3)
	v_mfma_f32_32x32x16_f16 v[30:45], v[110:113], v[58:61], v[30:45]
	v_pk_add_f16 v48, v18, v146
	v_pk_add_f16 v49, v19, v147
	s_nop 0
	v_pk_mul_f16 v46, v20, v148 clamp
	v_pk_mul_f16 v47, v21, v149 clamp
	v_pk_max_f16 v46, v48, v46
	v_pk_max_f16 v47, v49, v47
	ds_write_b64 v189, v[46:47] offset:33792
	s_waitcnt vmcnt(3) lgkmcnt(3)
	v_mfma_f32_32x32x16_f16 v[30:45], v[94:97], v[162:165], v[30:45]
	v_pk_add_f16 v48, v18, v138
	v_pk_add_f16 v49, v19, v139
	s_nop 0
	v_pk_mul_f16 v46, v20, v140 clamp
	v_pk_mul_f16 v47, v21, v141 clamp
	v_pk_max_f16 v46, v48, v46
	v_pk_max_f16 v47, v49, v47
	ds_write_b64 v189, v[46:47] offset:34320
	s_waitcnt vmcnt(2) lgkmcnt(3)
	v_mfma_f32_32x32x16_f16 v[30:45], v[134:137], v[22:25], v[30:45]
	v_pk_add_f16 v48, v18, v150
	v_pk_add_f16 v49, v19, v151
	s_nop 0
	v_pk_mul_f16 v46, v20, v152 clamp
	v_pk_mul_f16 v47, v21, v153 clamp
	v_pk_max_f16 v46, v48, v46
	v_pk_max_f16 v47, v49, v47
	ds_write_b64 v189, v[46:47] offset:34848
	s_waitcnt vmcnt(1) lgkmcnt(3)
	v_mfma_f32_32x32x16_f16 v[30:45], v[130:133], v[26:29], v[30:45]
	v_pk_add_f16 v22, v18, v142
	v_pk_add_f16 v23, v19, v143
	s_nop 0
	v_pk_mul_f16 v18, v20, v144 clamp
	v_pk_mul_f16 v19, v21, v145 clamp
	v_pk_max_f16 v18, v22, v18
	v_pk_max_f16 v19, v23, v19
	ds_write_b64 v189, v[18:19] offset:35376
	global_load_dwordx4 v[162:165], v[154:155], off
	ds_read_b128 v[46:49], v179 offset:16896
	ds_read_b128 v[50:53], v179 offset:16928
	ds_read_b128 v[54:57], v179 offset:16960
	ds_read_b128 v[58:61], v179 offset:16992
	ds_read_b128 v[168:171], v179 offset:17024
	ds_read_b128 v[172:175], v179 offset:17056
	s_nop 0
	v_cvt_pk_f16_f32 v167, v30, v31
	v_cvt_pk_f16_f32 v177, v32, v33
	s_waitcnt lgkmcnt(5)
	v_mfma_f32_32x32x16_f16 v[18:33], v[122:125], v[46:49], v[2:17]
	ds_read_b128 v[180:183], v179 offset:17088
	s_waitcnt lgkmcnt(5)
	v_mfma_f32_32x32x16_f16 v[18:33], v[98:101], v[50:53], v[18:33]
	ds_read_b128 v[184:187], v179 offset:17120
	v_exp_f16_e64 v46, v167 clamp
	v_exp_f16_e64 v47, v177 clamp
	v_exp_f16_sdwa v46, v167 clamp dst_sel:WORD_1 dst_unused:UNUSED_PRESERVE src0_sel:WORD_1
	v_exp_f16_sdwa v47, v177 clamp dst_sel:WORD_1 dst_unused:UNUSED_PRESERVE src0_sel:WORD_1
	s_nop 0
	s_waitcnt lgkmcnt(5)
	v_mfma_f32_32x32x16_f16 v[18:33], v[114:117], v[54:57], v[18:33]
	ds_read_b128 v[190:193], v179 offset:17152
	s_movk_i32 s0, 0x3dc5
	v_mov_b32_e32 v178, 0xbdc5
	v_pk_fma_f16 v47, v47, s0, v178 op_sel_hi:[1,0,0]
	v_pk_fma_f16 v46, v46, s0, v178 op_sel_hi:[1,0,0]
	v_pk_max_f16 v47, v177, v47
	v_pk_max_f16 v46, v167, v46
	s_waitcnt lgkmcnt(5)
	v_mfma_f32_32x32x16_f16 v[18:33], v[86:89], v[58:61], v[18:33]
	ds_read_b128 v[194:197], v179 offset:17184
	v_cvt_pk_f16_f32 v48, v34, v35
	v_cvt_pk_f16_f32 v49, v36, v37
	s_waitcnt lgkmcnt(5)
	v_mfma_f32_32x32x16_f16 v[18:33], v[126:129], v[168:171], v[18:33]
	ds_read_b128 v[34:37], v179 offset:17216
	v_exp_f16_e64 v50, v48 clamp
	v_exp_f16_e64 v51, v49 clamp
	v_exp_f16_sdwa v50, v48 clamp dst_sel:WORD_1 dst_unused:UNUSED_PRESERVE src0_sel:WORD_1
	v_exp_f16_sdwa v51, v49 clamp dst_sel:WORD_1 dst_unused:UNUSED_PRESERVE src0_sel:WORD_1
	s_nop 0
	s_waitcnt lgkmcnt(5)
	v_mfma_f32_32x32x16_f16 v[18:33], v[90:93], v[172:175], v[18:33]
	ds_read_b128 v[168:171], v179 offset:17248
	v_pk_fma_f16 v51, v51, s0, v178 op_sel_hi:[1,0,0]
	v_pk_fma_f16 v50, v50, s0, v178 op_sel_hi:[1,0,0]
	v_pk_max_f16 v49, v49, v51
	v_pk_max_f16 v48, v48, v50
	s_waitcnt lgkmcnt(5)
	v_mfma_f32_32x32x16_f16 v[18:33], v[118:121], v[180:183], v[18:33]
	ds_read_b128 v[172:175], v179 offset:17280
	v_cvt_pk_f16_f32 v167, v38, v39
	v_cvt_pk_f16_f32 v177, v40, v41
	v_mfma_f32_16x16x32_f16 v[58:61], v[70:73], v[46:49], 0
	s_waitcnt lgkmcnt(5)
	v_mfma_f32_32x32x16_f16 v[18:33], v[78:81], v[184:187], v[18:33]
	ds_read_b128 v[38:41], v179 offset:17312
	v_exp_f16_e64 v188, v167 clamp
	v_exp_f16_e64 v198, v177 clamp
	v_exp_f16_sdwa v188, v167 clamp dst_sel:WORD_1 dst_unused:UNUSED_PRESERVE src0_sel:WORD_1
	v_exp_f16_sdwa v198, v177 clamp dst_sel:WORD_1 dst_unused:UNUSED_PRESERVE src0_sel:WORD_1
	s_nop 0
	s_waitcnt lgkmcnt(5)
	v_mfma_f32_32x32x16_f16 v[18:33], v[102:105], v[190:193], v[18:33]
	ds_read_b128 v[180:183], v179 offset:17344
	v_pk_fma_f16 v184, v198, s0, v178 op_sel_hi:[1,0,0]
	s_nop 0
	v_pk_max_f16 v185, v177, v184
	v_pk_fma_f16 v177, v188, s0, v178 op_sel_hi:[1,0,0]
	s_nop 0
	v_pk_max_f16 v184, v167, v177
	s_waitcnt lgkmcnt(5)
	v_mfma_f32_32x32x16_f16 v[18:33], v[74:77], v[194:197], v[18:33]
	ds_read_b128 v[190:193], v179 offset:17376
	v_cvt_pk_f16_f32 v42, v42, v43
	v_cvt_pk_f16_f32 v43, v44, v45
	s_waitcnt lgkmcnt(5)
	v_mfma_f32_32x32x16_f16 v[18:33], v[106:109], v[34:37], v[18:33]
	v_exp_f16_e64 v44, v42 clamp
	v_exp_f16_e64 v45, v43 clamp
	v_exp_f16_sdwa v44, v42 clamp dst_sel:WORD_1 dst_unused:UNUSED_PRESERVE src0_sel:WORD_1
	v_exp_f16_sdwa v45, v43 clamp dst_sel:WORD_1 dst_unused:UNUSED_PRESERVE src0_sel:WORD_1
	s_nop 0
	s_waitcnt lgkmcnt(4)
	v_mfma_f32_32x32x16_f16 v[18:33], v[82:85], v[168:171], v[18:33]
	v_pk_fma_f16 v34, v45, s0, v178 op_sel_hi:[1,0,0]
	s_nop 0
	v_pk_max_f16 v187, v43, v34
	v_pk_fma_f16 v34, v44, s0, v178 op_sel_hi:[1,0,0]
	s_nop 0
	v_pk_max_f16 v186, v42, v34
	s_waitcnt lgkmcnt(3)
	v_mfma_f32_32x32x16_f16 v[18:33], v[110:113], v[172:175], v[18:33]
	v_pk_add_f16 v36, v62, v146
	v_pk_add_f16 v37, v63, v147
	s_nop 0
	v_pk_mul_f16 v34, v64, v148 clamp
	v_pk_mul_f16 v35, v65, v149 clamp
	v_pk_max_f16 v34, v36, v34
	v_pk_max_f16 v35, v37, v35
	ds_write_b64 v189, v[34:35] offset:50688
	v_mfma_f32_16x16x32_f16 v[58:61], v[66:69], v[184:187], v[58:61]
	s_waitcnt lgkmcnt(3)
	v_mfma_f32_32x32x16_f16 v[18:33], v[94:97], v[38:41], v[18:33]
	v_pk_add_f16 v36, v62, v138
	v_pk_add_f16 v37, v63, v139
	s_nop 0
	v_pk_mul_f16 v34, v64, v140 clamp
	v_pk_mul_f16 v35, v65, v141 clamp
	v_pk_max_f16 v34, v36, v34
	v_pk_max_f16 v35, v37, v35
	ds_write_b64 v189, v[34:35] offset:51216
	s_waitcnt lgkmcnt(3)
	v_mfma_f32_32x32x16_f16 v[18:33], v[134:137], v[180:183], v[18:33]
	v_pk_add_f16 v36, v62, v150
	v_pk_add_f16 v37, v63, v151
	s_nop 0
	v_pk_mul_f16 v34, v64, v152 clamp
	v_pk_mul_f16 v35, v65, v153 clamp
	v_pk_max_f16 v34, v36, v34
	v_pk_max_f16 v35, v37, v35
	ds_write_b64 v189, v[34:35] offset:51744
	s_waitcnt lgkmcnt(3)
	v_mfma_f32_32x32x16_f16 v[18:33], v[130:133], v[190:193], v[18:33]
	v_pk_add_f16 v36, v62, v142
	v_pk_add_f16 v37, v63, v143
	s_nop 0
	v_pk_mul_f16 v34, v64, v144 clamp
	v_pk_mul_f16 v35, v65, v145 clamp
	v_pk_max_f16 v34, v36, v34
	v_pk_max_f16 v35, v37, v35
	ds_write_b64 v189, v[34:35] offset:52272
	v_and_b32_e32 v157, 15, v199
	v_lshrrev_b32_e32 v1, 5, v199
	v_lshl_or_b32 v157, v1, 4, v157
	v_bfe_u32 v1, v199, 4, 1
	v_lshlrev_b32_e32 v1, 2, v1
	v_or_b32_e32 v178, s2, v157
	v_mul_lo_u32 v167, v178, 7
	v_add_u32_e32 v170, v167, v1
	v_mov_b32_e32 v34, 0x10800
	v_lshl_add_u32 v206, v170, 2, v34
	v_and_b32_e32 v34, 16, v199
	v_cmp_eq_u32_e64 s[0:1], 0, v34
	v_mov_b32_e32 v34, 0x10808
	v_lshl_add_u32 v34, v167, 2, v34
	v_or_b32_e32 v36, 3, v1
	v_mul_i32_i24_e32 v34, -6, v156
	v_mul_u32_u24_e32 v35, 7, v156
	v_cmp_gt_u32_e64 s[2:3], 6, v36
	v_lshlrev_b32_e32 v171, 2, v167
	v_lshlrev_b32_e32 v172, 2, v36
	s_mov_b32 s5, 0x10800
	v_add3_u32 v36, v171, v172, s5
	ds_write2_b32 v206, v58, v59 offset1:1
	s_and_saveexec_b64 s[2:3], s[0:1]
	ds_write2_b32 v206, v60, v61 offset0:2 offset1:3
	s_or_b64 exec, exec, s[2:3]
	s_sub_i32 s9, 0xff, s28
	s_mul_i32 s9, s9, s28
	s_not_b32 s25, s28
	s_ashr_i32 s9, s9, 1
	s_add_i32 s24, s24, s25
	s_add_i32 s24, s24, s9
	s_mul_i32 s8, s39, 0x1fc0
	s_ashr_i32 s9, s24, 31
	s_mul_hi_u32 s5, s39, 0x1fc0
	s_add_u32 s8, s8, s24
	s_addc_u32 s5, s5, s9
	s_mul_i32 s5, s5, 6
	s_mul_hi_u32 s9, s8, 6
	s_add_i32 s9, s9, s5
	v_add_u32_e32 v34, v34, v0
	s_cmpk_lt_u32 s21, 0xc0
	v_add_u32_e32 v173, v34, v35
	v_lshl_or_b32 v177, v34, 8, v156
	s_mul_i32 s8, s8, 6
	s_cselect_b64 s[24:25], -1, 0
	s_cmpk_gt_u32 s21, 0xbf
	s_waitcnt lgkmcnt(0)
	s_barrier
	s_cbranch_scc1 .LBB1_33
	s_andn2_b64 vcc, exec, s[6:7]
	s_mov_b64 s[6:7], -1
	s_cbranch_vccnz .LBB1_29
	s_movk_i32 s5, 0x60
	v_cmp_gt_u32_e32 vcc, s5, v0
	s_and_saveexec_b64 s[6:7], vcc
	s_cbranch_execz .LBB1_28
	v_lshlrev_b32_e32 v38, 2, v173
	v_add_u32_e32 v46, 0x10800, v38
	ds_read2_b32 v[34:35], v46 offset1:224
	v_add_u32_e32 v36, 0x700, v46
	ds_read2_b32 v[36:37], v36 offset1:224
	v_add_u32_e32 v39, 0x109c0, v38
	v_add_u32_e32 v40, 0x10d40, v38
	v_add_u32_e32 v41, 0x110c0, v38
	v_add_u32_e32 v42, 0x11440, v38
	v_add_u32_e32 v43, 0x117c0, v38
	v_add_u32_e32 v44, 0x11b40, v38
	v_add_u32_e32 v45, 0x11ec0, v38
	v_add_u32_e32 v47, 0x12240, v38
	s_waitcnt lgkmcnt(1)
	s_lshl_b64 s[26:27], s[8:9], 2
	v_add_f32_e32 v34, 0, v34
	v_add_f32_e32 v38, v34, v35
	s_waitcnt lgkmcnt(0)
	v_mov_b64_e32 v[34:35], v[36:37]
	v_add_u32_e32 v36, 0xe00, v46
	ds_read2_b32 v[36:37], v36 offset1:224
	v_add_f32_e32 v34, v38, v34
	v_add_u32_e32 v38, 0x1500, v46
	ds_read2_b32 v[38:39], v38 offset1:224
	v_add_f32_e32 v40, v34, v35
	s_waitcnt lgkmcnt(1)
	v_mov_b64_e32 v[34:35], v[36:37]
	s_add_u32 s26, s10, s26
	v_add_f32_e32 v34, v40, v34
	v_add_f32_e32 v36, v34, v35
	s_waitcnt lgkmcnt(0)
	v_mov_b64_e32 v[34:35], v[38:39]
	s_addc_u32 s27, s11, s27
	v_add_f32_e32 v34, v36, v34
	v_add_f32_e32 v34, v34, v35
	v_fmamk_f32 v34, v34, 0x3eb17218, v176
	v_lshlrev_b32 v35, 2, v0
	global_store_dword v35, v34, s[26:27]

.LBB1_46:
.LBB1_47:
	s_and_saveexec_b64 s[28:29], s[4:5]
	s_cbranch_execz .LBB1_49
	ds_read2_b32 v[34:35], v200 offset1:224
	ds_read2_b32 v[36:37], v234 offset1:224
	s_waitcnt lgkmcnt(1)
	s_waitcnt lgkmcnt(0)
	v_add_f32_e32 v34, 0, v34
	v_add_f32_e32 v38, v34, v35
	ds_read2_b32 v[34:35], v235 offset1:224
	v_add_f32_e32 v36, v38, v36
	ds_read2_b32 v[38:39], v236 offset1:224
	v_add_f32_e32 v36, v36, v37
	s_lshl_b64 s[34:35], s[26:27], 2
	s_waitcnt lgkmcnt(1)
	s_add_u32 s34, s10, s34
	v_add_f32_e32 v34, v36, v34
	v_add_f32_e32 v36, v34, v35
	s_waitcnt lgkmcnt(0)
	v_mov_b64_e32 v[34:35], v[38:39]
	s_addc_u32 s35, s11, s35
	v_add_f32_e32 v34, v36, v34
	v_add_f32_e32 v34, v34, v35
	v_fmamk_f32 v34, v34, 0x3eb17218, v176
	v_lshlrev_b32 v35, 2, v0
	global_store_dword v35, v34, s[34:35]

.LBB1_55:
.LBB1_56:
	s_and_saveexec_b64 s[28:29], s[4:5]
	s_cbranch_execz .LBB1_58
	ds_read2_b32 v[34:35], v190 offset1:224
	ds_read2_b32 v[36:37], v237 offset1:224
	s_waitcnt lgkmcnt(1)
	s_waitcnt lgkmcnt(0)
	v_add_f32_e32 v34, 0, v34
	v_add_f32_e32 v38, v34, v35
	ds_read2_b32 v[34:35], v238 offset1:224
	v_add_f32_e32 v36, v38, v36
	ds_read2_b32 v[38:39], v239 offset1:224
	v_add_f32_e32 v36, v36, v37
	s_lshl_b64 s[34:35], s[26:27], 2
	s_waitcnt lgkmcnt(1)
	s_add_u32 s34, s10, s34
	v_add_f32_e32 v34, v36, v34
	v_add_f32_e32 v36, v34, v35
	s_waitcnt lgkmcnt(0)
	v_mov_b64_e32 v[34:35], v[38:39]
	s_addc_u32 s35, s11, s35
	v_add_f32_e32 v34, v36, v34
	v_add_f32_e32 v34, v34, v35
	v_fmamk_f32 v34, v34, 0x3eb17218, v176
	v_lshlrev_b32 v35, 2, v0
	global_store_dword v35, v34, s[34:35]

.LBB1_72:
.LBB1_73:
	s_and_saveexec_b64 s[28:29], s[4:5]
	s_cbranch_execz .LBB1_75
	ds_read2_b32 v[34:35], v180 offset1:224
	v_add_u32_e32 v36, 0x700, v180
	ds_read2_b32 v[36:37], v36 offset1:224
	s_lshl_b64 s[34:35], s[26:27], 2
	s_add_u32 s34, s10, s34
	s_waitcnt lgkmcnt(1)
	s_addc_u32 s35, s11, s35
	v_add_f32_e32 v34, 0, v34
	v_add_f32_e32 v38, v34, v35
	s_waitcnt lgkmcnt(0)
	v_mov_b64_e32 v[34:35], v[36:37]
	v_add_u32_e32 v36, 0xe00, v180
	ds_read2_b32 v[36:37], v36 offset1:224
	v_add_f32_e32 v34, v38, v34
	v_add_u32_e32 v38, 0x1500, v180
	ds_read2_b32 v[38:39], v38 offset1:224
	v_add_f32_e32 v40, v34, v35
	s_waitcnt lgkmcnt(1)
	v_mov_b64_e32 v[34:35], v[36:37]
	s_nop 0
	v_add_f32_e32 v34, v40, v34
	v_add_f32_e32 v36, v34, v35
	s_waitcnt lgkmcnt(0)
	v_mov_b64_e32 v[34:35], v[38:39]
	s_nop 0
	v_add_f32_e32 v34, v36, v34
	v_add_f32_e32 v34, v34, v35
	v_fmamk_f32 v34, v34, 0x3eb17218, v176
	v_lshlrev_b32 v35, 2, v0
	global_store_dword v35, v34, s[34:35]

.LBB1_81:
.LBB1_82:
	s_and_saveexec_b64 s[26:27], s[4:5]
	s_cbranch_execz .LBB1_84
	ds_read2_b32 v[34:35], v216 offset1:224
	v_add_u32_e32 v36, 0x700, v216
	ds_read2_b32 v[36:37], v36 offset1:224
	s_lshl_b64 s[30:31], s[28:29], 2
	s_add_u32 s30, s10, s30
	s_waitcnt lgkmcnt(1)
	s_addc_u32 s31, s11, s31
	v_add_f32_e32 v34, 0, v34
	v_add_f32_e32 v38, v34, v35
	s_waitcnt lgkmcnt(0)
	v_mov_b64_e32 v[34:35], v[36:37]
	v_add_u32_e32 v36, 0xe00, v216
	ds_read2_b32 v[36:37], v36 offset1:224
	v_add_f32_e32 v34, v38, v34
	v_add_u32_e32 v38, 0x1500, v216
	ds_read2_b32 v[38:39], v38 offset1:224
	v_add_f32_e32 v40, v34, v35
	s_waitcnt lgkmcnt(1)
	v_mov_b64_e32 v[34:35], v[36:37]
	s_nop 0
	v_add_f32_e32 v34, v40, v34
	v_add_f32_e32 v36, v34, v35
	s_waitcnt lgkmcnt(0)
	v_mov_b64_e32 v[34:35], v[38:39]
	s_nop 0
	v_add_f32_e32 v34, v36, v34
	v_add_f32_e32 v34, v34, v35
	v_fmamk_f32 v34, v34, 0x3eb17218, v176
	v_lshlrev_b32 v35, 2, v0
	global_store_dword v35, v34, s[30:31]

.LBB1_106:
.LBB1_107:
	s_and_saveexec_b64 s[30:31], s[4:5]
	s_cbranch_execz .LBB1_109
	ds_read2_b32 v[34:35], v200 offset1:224
	ds_read2_b32 v[36:37], v234 offset1:224
	s_waitcnt lgkmcnt(1)
	s_waitcnt lgkmcnt(0)
	v_add_f32_e32 v34, 0, v34
	v_add_f32_e32 v38, v34, v35
	ds_read2_b32 v[34:35], v235 offset1:224
	v_add_f32_e32 v36, v38, v36
	ds_read2_b32 v[38:39], v236 offset1:224
	v_add_f32_e32 v36, v36, v37
	s_lshl_b64 s[36:37], s[28:29], 2
	s_waitcnt lgkmcnt(1)
	s_add_u32 s36, s10, s36
	v_add_f32_e32 v34, v36, v34
	v_add_f32_e32 v36, v34, v35
	s_waitcnt lgkmcnt(0)
	v_mov_b64_e32 v[34:35], v[38:39]
	s_addc_u32 s37, s11, s37
	v_add_f32_e32 v34, v36, v34
	v_add_f32_e32 v34, v34, v35
	v_fmamk_f32 v34, v34, 0x3eb17218, v176
	v_lshlrev_b32 v35, 2, v0
	global_store_dword v35, v34, s[36:37]

.LBB1_115:
.LBB1_116:
	s_and_saveexec_b64 s[30:31], s[4:5]
	s_cbranch_execz .LBB1_118
	ds_read2_b32 v[34:35], v190 offset1:224
	ds_read2_b32 v[36:37], v237 offset1:224
	s_waitcnt lgkmcnt(1)
	s_waitcnt lgkmcnt(0)
	v_add_f32_e32 v34, 0, v34
	v_add_f32_e32 v38, v34, v35
	ds_read2_b32 v[34:35], v238 offset1:224
	v_add_f32_e32 v36, v38, v36
	ds_read2_b32 v[38:39], v239 offset1:224
	v_add_f32_e32 v36, v36, v37
	s_lshl_b64 s[36:37], s[28:29], 2
	s_waitcnt lgkmcnt(1)
	s_add_u32 s36, s10, s36
	v_add_f32_e32 v34, v36, v34
	v_add_f32_e32 v36, v34, v35
	s_waitcnt lgkmcnt(0)
	v_mov_b64_e32 v[34:35], v[38:39]
	s_addc_u32 s37, s11, s37
	v_add_f32_e32 v34, v36, v34
	v_add_f32_e32 v34, v34, v35
	v_fmamk_f32 v34, v34, 0x3eb17218, v176
	v_lshlrev_b32 v35, 2, v0
	global_store_dword v35, v34, s[36:37]

.LBB1_119:
	v_lshl_add_u64 v[154:155], s[20:21], 4, v[158:159]
	global_load_dwordx4 v[158:161], v[154:155], off
	s_waitcnt lgkmcnt(5)
	v_mfma_f32_32x32x16_f16 v[34:49], v[122:125], v[50:53], v[2:17]
	ds_read_b128 v[244:247], v179 offset:192
	v_cvt_pk_f16_f32 v156, v18, v19
	v_cvt_pk_f16_f32 v157, v20, v21
	s_waitcnt lgkmcnt(5)
	v_mfma_f32_32x32x16_f16 v[34:49], v[98:101], v[54:57], v[34:49]
	ds_read_b128 v[18:21], v179 offset:224
	v_exp_f16_e64 v50, v156 clamp
	v_exp_f16_e64 v51, v157 clamp
	v_exp_f16_sdwa v50, v156 clamp dst_sel:WORD_1 dst_unused:UNUSED_PRESERVE src0_sel:WORD_1
	v_exp_f16_sdwa v51, v157 clamp dst_sel:WORD_1 dst_unused:UNUSED_PRESERVE src0_sel:WORD_1
	s_nop 0
	s_waitcnt lgkmcnt(5)
	v_mfma_f32_32x32x16_f16 v[34:49], v[114:117], v[58:61], v[34:49]
	ds_read_b128 v[248:251], v179 offset:256
	v_pk_fma_f16 v51, v51, s55, v233 op_sel_hi:[1,0,0]
	v_pk_fma_f16 v50, v50, s55, v233 op_sel_hi:[1,0,0]
	v_pk_max_f16 v51, v157, v51
	v_pk_max_f16 v50, v156, v50
	s_waitcnt lgkmcnt(5)
	v_mfma_f32_32x32x16_f16 v[34:49], v[86:89], v[62:65], v[34:49]
	ds_read_b128 v[252:255], v179 offset:288
	v_cvt_pk_f16_f32 v52, v22, v23
	v_cvt_pk_f16_f32 v53, v24, v25
	s_waitcnt lgkmcnt(5)
	v_mfma_f32_32x32x16_f16 v[34:49], v[126:129], v[162:165], v[34:49]
	ds_read_b128 v[22:25], v179 offset:320
	v_exp_f16_e64 v54, v52 clamp
	v_exp_f16_e64 v55, v53 clamp
	v_exp_f16_sdwa v54, v52 clamp dst_sel:WORD_1 dst_unused:UNUSED_PRESERVE src0_sel:WORD_1
	v_exp_f16_sdwa v55, v53 clamp dst_sel:WORD_1 dst_unused:UNUSED_PRESERVE src0_sel:WORD_1
	s_nop 0
	s_waitcnt lgkmcnt(5)
	v_mfma_f32_32x32x16_f16 v[34:49], v[90:93], v[240:243], v[34:49]
	ds_read_b128 v[162:165], v179 offset:352
	v_pk_fma_f16 v55, v55, s55, v233 op_sel_hi:[1,0,0]
	v_pk_fma_f16 v54, v54, s55, v233 op_sel_hi:[1,0,0]
	v_pk_max_f16 v53, v53, v55
	v_pk_max_f16 v52, v52, v54
	s_waitcnt lgkmcnt(5)
	v_mfma_f32_32x32x16_f16 v[34:49], v[118:121], v[244:247], v[34:49]
	ds_read_b128 v[240:243], v179 offset:384
	v_cvt_pk_f16_f32 v156, v26, v27
	v_cvt_pk_f16_f32 v157, v28, v29
	v_mfma_f32_16x16x32_f16 v[62:65], v[70:73], v[50:53], 0
	s_waitcnt lgkmcnt(5)
	v_mfma_f32_32x32x16_f16 v[34:49], v[78:81], v[18:21], v[34:49]
	ds_read_b128 v[26:29], v179 offset:416
	v_exp_f16_e64 v244, v156 clamp
	v_exp_f16_e64 v245, v157 clamp
	v_exp_f16_sdwa v244, v156 clamp dst_sel:WORD_1 dst_unused:UNUSED_PRESERVE src0_sel:WORD_1
	v_exp_f16_sdwa v245, v157 clamp dst_sel:WORD_1 dst_unused:UNUSED_PRESERVE src0_sel:WORD_1
	s_nop 0
	s_waitcnt lgkmcnt(5)
	v_mfma_f32_32x32x16_f16 v[34:49], v[102:105], v[248:251], v[34:49]
	ds_read_b128 v[18:21], v179 offset:448
	v_pk_fma_f16 v245, v245, s55, v233 op_sel_hi:[1,0,0]
	s_nop 0
	v_pk_max_f16 v245, v157, v245
	v_pk_fma_f16 v157, v244, s55, v233 op_sel_hi:[1,0,0]
	s_nop 0
	v_pk_max_f16 v244, v156, v157
	s_waitcnt lgkmcnt(5)
	v_mfma_f32_32x32x16_f16 v[34:49], v[74:77], v[252:255], v[34:49]
	ds_read_b128 v[248:251], v179 offset:480
	v_cvt_pk_f16_f32 v30, v30, v31
	v_cvt_pk_f16_f32 v31, v32, v33
	s_waitcnt lgkmcnt(5)
	v_mfma_f32_32x32x16_f16 v[34:49], v[106:109], v[22:25], v[34:49]
	v_exp_f16_e64 v32, v30 clamp
	v_exp_f16_e64 v33, v31 clamp
	v_exp_f16_sdwa v32, v30 clamp dst_sel:WORD_1 dst_unused:UNUSED_PRESERVE src0_sel:WORD_1
	v_exp_f16_sdwa v33, v31 clamp dst_sel:WORD_1 dst_unused:UNUSED_PRESERVE src0_sel:WORD_1
	s_nop 0
	s_waitcnt lgkmcnt(4)
	v_mfma_f32_32x32x16_f16 v[34:49], v[82:85], v[162:165], v[34:49]
	v_pk_fma_f16 v22, v33, s55, v233 op_sel_hi:[1,0,0]
	s_nop 0
	v_pk_max_f16 v247, v31, v22
	v_pk_fma_f16 v22, v32, s55, v233 op_sel_hi:[1,0,0]
	s_nop 0
	v_pk_max_f16 v246, v30, v22
	s_waitcnt lgkmcnt(3)
	v_mfma_f32_32x32x16_f16 v[34:49], v[110:113], v[240:243], v[34:49]
	s_waitcnt vmcnt(2)
	v_pk_add_f16 v24, v170, v146
	v_pk_add_f16 v25, v171, v147
	s_nop 0
	v_pk_mul_f16 v22, v172, v148 clamp
	v_pk_mul_f16 v23, v173, v149 clamp
	v_pk_max_f16 v22, v24, v22
	v_pk_max_f16 v23, v25, v23
	ds_write_b64 v189, v[22:23] offset:33792
	v_mfma_f32_16x16x32_f16 v[62:65], v[66:69], v[244:247], v[62:65]
	s_waitcnt lgkmcnt(3)
	v_mfma_f32_32x32x16_f16 v[34:49], v[94:97], v[26:29], v[34:49]
	v_pk_add_f16 v24, v170, v138
	v_pk_add_f16 v25, v171, v139
	s_nop 0
	v_pk_mul_f16 v22, v172, v140 clamp
	v_pk_mul_f16 v23, v173, v141 clamp
	v_pk_max_f16 v22, v24, v22
	v_pk_max_f16 v23, v25, v23
	ds_write_b64 v189, v[22:23] offset:34320
	s_waitcnt lgkmcnt(3)
	v_mfma_f32_32x32x16_f16 v[34:49], v[134:137], v[18:21], v[34:49]
	v_pk_add_f16 v24, v170, v150
	v_pk_add_f16 v25, v171, v151
	s_nop 0
	v_pk_mul_f16 v22, v172, v152 clamp
	v_pk_mul_f16 v23, v173, v153 clamp
	v_pk_max_f16 v22, v24, v22
	v_pk_max_f16 v23, v25, v23
	ds_write_b64 v189, v[22:23] offset:34848
	s_waitcnt lgkmcnt(3)
	v_mfma_f32_32x32x16_f16 v[34:49], v[130:133], v[248:251], v[34:49]
	v_pk_add_f16 v20, v170, v142
	v_pk_add_f16 v21, v171, v143
	s_nop 0
	v_pk_mul_f16 v18, v172, v144 clamp
	v_pk_mul_f16 v19, v173, v145 clamp
	v_pk_max_f16 v18, v20, v18
	v_pk_max_f16 v19, v21, v19
	ds_write_b64 v189, v[18:19] offset:35376
	ds_write2_b32 v229, v62, v63 offset1:1
	s_and_saveexec_b64 s[30:31], s[0:1]
	ds_write2_b32 v229, v64, v65 offset0:2 offset1:3
	s_or_b64 exec, exec, s[30:31]
	s_cmp_eq_u32 s56, 16
	s_cbranch_scc0 .Lw2_sw_skip
	s_and_b64 vcc, exec, s[16:17]
	s_cbranch_vccz .Lw2_sw_skip
	v_mov_b32_dpp v70, v70 row_shl:8 row_mask:0xa bank_mask:0x3
	v_mov_b32_dpp v71, v71 row_shl:8 row_mask:0xa bank_mask:0x3
	v_mov_b32_dpp v72, v72 row_shl:8 row_mask:0xa bank_mask:0x3
	v_mov_b32_dpp v73, v73 row_shl:8 row_mask:0xa bank_mask:0x3
	v_mov_b32_dpp v66, v66 row_shl:8 row_mask:0xa bank_mask:0x3
	v_mov_b32_dpp v67, v67 row_shl:8 row_mask:0xa bank_mask:0x3
	v_mov_b32_dpp v68, v68 row_shl:8 row_mask:0xa bank_mask:0x3
	v_mov_b32_dpp v69, v69 row_shl:8 row_mask:0xa bank_mask:0x3
.Lw2_sw_skip:
	v_lshl_add_u64 v[154:155], s[20:21], 4, v[154:155]
	global_load_dwordx4 v[162:165], v[154:155], off
	ds_read_b128 v[50:53], v179 offset:16896
	ds_read_b128 v[54:57], v179 offset:16928
	ds_read_b128 v[58:61], v179 offset:16960
	ds_read_b128 v[62:65], v179 offset:16992
	ds_read_b128 v[170:173], v179 offset:17024
	ds_read_b128 v[240:243], v179 offset:17056
	s_waitcnt lgkmcnt(5)
	v_mfma_f32_32x32x16_f16 v[18:33], v[122:125], v[50:53], v[2:17]
	ds_read_b128 v[244:247], v179 offset:17088
	v_cvt_pk_f16_f32 v156, v34, v35
	v_cvt_pk_f16_f32 v157, v36, v37
	s_waitcnt lgkmcnt(5)
	v_mfma_f32_32x32x16_f16 v[18:33], v[98:101], v[54:57], v[18:33]
	ds_read_b128 v[34:37], v179 offset:17120
	v_exp_f16_e64 v50, v156 clamp
	v_exp_f16_e64 v51, v157 clamp
	v_exp_f16_sdwa v50, v156 clamp dst_sel:WORD_1 dst_unused:UNUSED_PRESERVE src0_sel:WORD_1
	v_exp_f16_sdwa v51, v157 clamp dst_sel:WORD_1 dst_unused:UNUSED_PRESERVE src0_sel:WORD_1
	s_nop 0
	s_waitcnt lgkmcnt(5)
	v_mfma_f32_32x32x16_f16 v[18:33], v[114:117], v[58:61], v[18:33]
	ds_read_b128 v[248:251], v179 offset:17152
	v_pk_fma_f16 v51, v51, s55, v233 op_sel_hi:[1,0,0]
	v_pk_fma_f16 v50, v50, s55, v233 op_sel_hi:[1,0,0]
	v_pk_max_f16 v51, v157, v51
	v_pk_max_f16 v50, v156, v50
	s_waitcnt lgkmcnt(5)
	v_mfma_f32_32x32x16_f16 v[18:33], v[86:89], v[62:65], v[18:33]
	ds_read_b128 v[252:255], v179 offset:17184
	v_cvt_pk_f16_f32 v52, v38, v39
	v_cvt_pk_f16_f32 v53, v40, v41
	s_waitcnt lgkmcnt(5)
	v_mfma_f32_32x32x16_f16 v[18:33], v[126:129], v[170:173], v[18:33]
	ds_read_b128 v[38:41], v179 offset:17216
	v_exp_f16_e64 v54, v52 clamp
	v_exp_f16_e64 v55, v53 clamp
	v_exp_f16_sdwa v54, v52 clamp dst_sel:WORD_1 dst_unused:UNUSED_PRESERVE src0_sel:WORD_1
	v_exp_f16_sdwa v55, v53 clamp dst_sel:WORD_1 dst_unused:UNUSED_PRESERVE src0_sel:WORD_1
	s_nop 0
	s_waitcnt lgkmcnt(5)
	v_mfma_f32_32x32x16_f16 v[18:33], v[90:93], v[240:243], v[18:33]
	ds_read_b128 v[170:173], v179 offset:17248
	v_pk_fma_f16 v55, v55, s55, v233 op_sel_hi:[1,0,0]
	v_pk_fma_f16 v54, v54, s55, v233 op_sel_hi:[1,0,0]
	v_pk_max_f16 v53, v53, v55
	v_pk_max_f16 v52, v52, v54
	s_waitcnt lgkmcnt(5)
	v_mfma_f32_32x32x16_f16 v[18:33], v[118:121], v[244:247], v[18:33]
	ds_read_b128 v[240:243], v179 offset:17280
	v_cvt_pk_f16_f32 v156, v42, v43
	v_cvt_pk_f16_f32 v157, v44, v45
	v_mfma_f32_16x16x32_f16 v[62:65], v[70:73], v[50:53], 0
	s_waitcnt lgkmcnt(5)
	v_mfma_f32_32x32x16_f16 v[18:33], v[78:81], v[34:37], v[18:33]
	ds_read_b128 v[42:45], v179 offset:17312
	v_exp_f16_e64 v244, v156 clamp
	v_exp_f16_e64 v245, v157 clamp
	v_exp_f16_sdwa v244, v156 clamp dst_sel:WORD_1 dst_unused:UNUSED_PRESERVE src0_sel:WORD_1
	v_exp_f16_sdwa v245, v157 clamp dst_sel:WORD_1 dst_unused:UNUSED_PRESERVE src0_sel:WORD_1
	s_nop 0
	s_waitcnt lgkmcnt(5)
	v_mfma_f32_32x32x16_f16 v[18:33], v[102:105], v[248:251], v[18:33]
	ds_read_b128 v[34:37], v179 offset:17344
	v_pk_fma_f16 v245, v245, s55, v233 op_sel_hi:[1,0,0]
	s_nop 0
	v_pk_max_f16 v245, v157, v245
	v_pk_fma_f16 v157, v244, s55, v233 op_sel_hi:[1,0,0]
	s_nop 0
	v_pk_max_f16 v244, v156, v157
	s_waitcnt lgkmcnt(5)
	v_mfma_f32_32x32x16_f16 v[18:33], v[74:77], v[252:255], v[18:33]
	ds_read_b128 v[248:251], v179 offset:17376
	v_cvt_pk_f16_f32 v46, v46, v47
	v_cvt_pk_f16_f32 v47, v48, v49
	s_waitcnt lgkmcnt(5)
	v_mfma_f32_32x32x16_f16 v[18:33], v[106:109], v[38:41], v[18:33]
	v_exp_f16_e64 v48, v46 clamp
	v_exp_f16_e64 v49, v47 clamp
	v_exp_f16_sdwa v48, v46 clamp dst_sel:WORD_1 dst_unused:UNUSED_PRESERVE src0_sel:WORD_1
	v_exp_f16_sdwa v49, v47 clamp dst_sel:WORD_1 dst_unused:UNUSED_PRESERVE src0_sel:WORD_1
	s_nop 0
	s_waitcnt lgkmcnt(4)
	v_mfma_f32_32x32x16_f16 v[18:33], v[82:85], v[170:173], v[18:33]
	v_pk_fma_f16 v38, v49, s55, v233 op_sel_hi:[1,0,0]
	s_nop 0
	v_pk_max_f16 v247, v47, v38
	v_pk_fma_f16 v38, v48, s55, v233 op_sel_hi:[1,0,0]
	s_nop 0
	v_pk_max_f16 v246, v46, v38
	s_waitcnt lgkmcnt(3)
	v_mfma_f32_32x32x16_f16 v[18:33], v[110:113], v[240:243], v[18:33]
	s_waitcnt vmcnt(2)
	v_pk_add_f16 v40, v166, v146
	v_pk_add_f16 v41, v167, v147
	s_nop 0
	v_pk_mul_f16 v38, v168, v148 clamp
	v_pk_mul_f16 v39, v169, v149 clamp
	v_pk_max_f16 v38, v40, v38
	v_pk_max_f16 v39, v41, v39
	ds_write_b64 v189, v[38:39] offset:50688
	v_mfma_f32_16x16x32_f16 v[62:65], v[66:69], v[244:247], v[62:65]
	s_waitcnt lgkmcnt(3)
	v_mfma_f32_32x32x16_f16 v[18:33], v[94:97], v[42:45], v[18:33]
	v_pk_add_f16 v40, v166, v138
	v_pk_add_f16 v41, v167, v139
	s_nop 0
	v_pk_mul_f16 v38, v168, v140 clamp
	v_pk_mul_f16 v39, v169, v141 clamp
	v_pk_max_f16 v38, v40, v38
	v_pk_max_f16 v39, v41, v39
	ds_write_b64 v189, v[38:39] offset:51216
	s_waitcnt lgkmcnt(3)
	v_mfma_f32_32x32x16_f16 v[18:33], v[134:137], v[34:37], v[18:33]
	v_pk_add_f16 v40, v166, v150
	v_pk_add_f16 v41, v167, v151
	s_nop 0
	v_pk_mul_f16 v38, v168, v152 clamp
	v_pk_mul_f16 v39, v169, v153 clamp
	v_pk_max_f16 v38, v40, v38
	v_pk_max_f16 v39, v41, v39
	ds_write_b64 v189, v[38:39] offset:51744
	s_waitcnt lgkmcnt(3)
	v_mfma_f32_32x32x16_f16 v[18:33], v[130:133], v[248:251], v[18:33]
	v_pk_add_f16 v36, v166, v142
	v_pk_add_f16 v37, v167, v143
	s_nop 0
	v_pk_mul_f16 v34, v168, v144 clamp
	v_pk_mul_f16 v35, v169, v145 clamp
	v_pk_max_f16 v34, v36, v34
	v_pk_max_f16 v35, v37, v35
	ds_write_b64 v189, v[34:35] offset:52272
	ds_write2_b32 v206, v62, v63 offset1:1
	s_and_saveexec_b64 s[30:31], s[0:1]
	ds_write2_b32 v206, v64, v65 offset0:2 offset1:3
	s_or_b64 exec, exec, s[30:31]
	s_add_i32 s34, s34, 1
	s_sub_i32 s30, 0x7d, s34
	s_mul_i32 s30, s30, 6
	s_ashr_i32 s31, s30, 31
	s_add_u32 s28, s28, s30
	s_addc_u32 s29, s29, s31
	s_and_b64 vcc, exec, s[8:9]
	s_waitcnt lgkmcnt(0)
	s_barrier
	ds_read_b128 v[50:53], v179 offset:33792
	ds_read_b128 v[54:57], v179 offset:33824
	ds_read_b128 v[58:61], v179 offset:33856
	ds_read_b128 v[62:65], v179 offset:33888
	ds_read_b128 v[168:171], v179 offset:33920
	ds_read_b128 v[240:243], v179 offset:33952
	s_cbranch_vccnz .LBB1_136
	s_cmp_eq_u32 s41, 0
	s_cbranch_scc1 .LBB1_132
	s_and_saveexec_b64 s[30:31], s[6:7]
	s_cbranch_execz .LBB1_131
	ds_read2_b32 v[34:35], v180 offset1:224
	v_add_u32_e32 v36, 0x700, v180
	ds_read2_b32 v[36:37], v36 offset1:224
	v_add_u32_e32 v38, 0xe00, v180
	s_lshl_b32 s35, s56, 28
	s_waitcnt lgkmcnt(1)
	v_add_f32_e32 v34, 0, v34
	v_add_f32_e32 v40, v34, v35
	ds_read2_b32 v[34:35], v38 offset1:224
	v_add_u32_e32 v38, 0x1500, v180
	ds_read2_b32 v[38:39], v38 offset1:224
	s_waitcnt lgkmcnt(2)
	v_add_f32_e32 v36, v40, v36
	v_add_f32_e32 v36, v36, v37
	s_waitcnt lgkmcnt(1)
	v_add_f32_e32 v34, v36, v34
	s_add_i32 s35, s35, 0xf0000000
	v_add_f32_e32 v34, v34, v35
	s_ashr_i32 s35, s35, 31
	s_waitcnt lgkmcnt(0)
	v_add_f32_e32 v34, v34, v38
	s_and_b32 s35, s35, 0x1800
	v_add_f32_e32 v34, v34, v39
	v_add_u32_e32 v35, s35, v232
	ds_write_b32 v35, v34 offset:896

.LBB1_132:
.LBB1_133:
	s_and_saveexec_b64 s[30:31], s[4:5]
	s_cbranch_execz .LBB1_135
	ds_read2_b32 v[34:35], v180 offset1:224
	v_add_u32_e32 v36, 0x700, v180
	ds_read2_b32 v[36:37], v36 offset1:224
	s_lshl_b64 s[36:37], s[28:29], 2
	s_add_u32 s36, s10, s36
	s_waitcnt lgkmcnt(1)
	s_addc_u32 s37, s11, s37
	v_add_f32_e32 v34, 0, v34
	v_add_f32_e32 v38, v34, v35
	s_waitcnt lgkmcnt(0)
	v_mov_b64_e32 v[34:35], v[36:37]
	v_add_u32_e32 v36, 0xe00, v180
	ds_read2_b32 v[36:37], v36 offset1:224
	v_add_f32_e32 v34, v38, v34
	v_add_u32_e32 v38, 0x1500, v180
	ds_read2_b32 v[38:39], v38 offset1:224
	v_add_f32_e32 v40, v34, v35
	s_waitcnt lgkmcnt(1)
	v_mov_b64_e32 v[34:35], v[36:37]
	s_nop 0
	v_add_f32_e32 v34, v40, v34
	v_add_f32_e32 v36, v34, v35
	s_waitcnt lgkmcnt(0)
	v_mov_b64_e32 v[34:35], v[38:39]
	s_nop 0
	v_add_f32_e32 v34, v36, v34
	v_add_f32_e32 v34, v34, v35
	v_fmamk_f32 v34, v34, 0x3eb17218, v176
	v_lshlrev_b32 v35, 2, v0
	global_store_dword v35, v34, s[36:37]

.LBB1_141:
.LBB1_142:
	s_and_saveexec_b64 s[30:31], s[4:5]
	s_cbranch_execz .LBB1_144
	ds_read2_b32 v[34:35], v216 offset1:224
	v_add_u32_e32 v36, 0x700, v216
	ds_read2_b32 v[36:37], v36 offset1:224
	s_lshl_b64 s[36:37], s[28:29], 2
	s_add_u32 s36, s10, s36
	s_waitcnt lgkmcnt(1)
	s_addc_u32 s37, s11, s37
	v_add_f32_e32 v34, 0, v34
	v_add_f32_e32 v38, v34, v35
	s_waitcnt lgkmcnt(0)
	v_mov_b64_e32 v[34:35], v[36:37]
	v_add_u32_e32 v36, 0xe00, v216
	ds_read2_b32 v[36:37], v36 offset1:224
	v_add_f32_e32 v34, v38, v34
	v_add_u32_e32 v38, 0x1500, v216
	ds_read2_b32 v[38:39], v38 offset1:224
	v_add_f32_e32 v40, v34, v35
	s_waitcnt lgkmcnt(1)
	v_mov_b64_e32 v[34:35], v[36:37]
	s_nop 0
	v_add_f32_e32 v34, v40, v34
	v_add_f32_e32 v36, v34, v35
	s_waitcnt lgkmcnt(0)
	v_mov_b64_e32 v[34:35], v[38:39]
	s_nop 0
	v_add_f32_e32 v34, v36, v34
	v_add_f32_e32 v34, v34, v35
	v_fmamk_f32 v34, v34, 0x3eb17218, v176
	v_lshlrev_b32 v35, 2, v0
	global_store_dword v35, v34, s[36:37]

.LBB1_160:
.LBB1_161:
	s_and_saveexec_b64 s[12:13], s[4:5]
	s_cbranch_execz .LBB1_163
	ds_read2_b32 v[34:35], v200 offset1:224
	v_add_u32_e32 v36, 0x700, v200
	ds_read2_b32 v[36:37], v36 offset1:224
	s_lshl_b64 s[20:21], s[26:27], 2
	s_add_u32 s20, s10, s20
	s_waitcnt lgkmcnt(1)
	s_addc_u32 s21, s11, s21
	v_add_f32_e32 v34, 0, v34
	v_add_f32_e32 v38, v34, v35
	s_waitcnt lgkmcnt(0)
	v_mov_b64_e32 v[34:35], v[36:37]
	v_add_u32_e32 v36, 0xe00, v200
	ds_read2_b32 v[36:37], v36 offset1:224
	v_add_f32_e32 v34, v38, v34
	v_add_u32_e32 v38, 0x1500, v200
	ds_read2_b32 v[38:39], v38 offset1:224
	v_add_f32_e32 v40, v34, v35
	s_waitcnt lgkmcnt(1)
	v_mov_b64_e32 v[34:35], v[36:37]
	s_nop 0
	v_add_f32_e32 v34, v40, v34
	v_add_f32_e32 v36, v34, v35
	s_waitcnt lgkmcnt(0)
	v_mov_b64_e32 v[34:35], v[38:39]
	s_nop 0
	v_add_f32_e32 v34, v36, v34
	v_add_f32_e32 v34, v34, v35
	v_fmamk_f32 v34, v34, 0x3eb17218, v176
	v_lshlrev_b32 v35, 2, v0
	global_store_dword v35, v34, s[20:21]

.LBB1_169:
.LBB1_170:
	s_and_saveexec_b64 s[20:21], s[4:5]
	s_cbranch_execz .LBB1_172
	ds_read2_b32 v[34:35], v190 offset1:224
	v_add_u32_e32 v36, 0x700, v190
	ds_read2_b32 v[36:37], v36 offset1:224
	s_lshl_b64 s[22:23], s[12:13], 2
	s_add_u32 s22, s10, s22
	s_waitcnt lgkmcnt(1)
	s_addc_u32 s23, s11, s23
	v_add_f32_e32 v34, 0, v34
	v_add_f32_e32 v38, v34, v35
	s_waitcnt lgkmcnt(0)
	v_mov_b64_e32 v[34:35], v[36:37]
	v_add_u32_e32 v36, 0xe00, v190
	ds_read2_b32 v[36:37], v36 offset1:224
	v_add_f32_e32 v34, v38, v34
	v_add_u32_e32 v38, 0x1500, v190
	ds_read2_b32 v[38:39], v38 offset1:224
	v_add_f32_e32 v40, v34, v35
	s_waitcnt lgkmcnt(1)
	v_mov_b64_e32 v[34:35], v[36:37]
	s_nop 0
	v_add_f32_e32 v34, v40, v34
	v_add_f32_e32 v36, v34, v35
	s_waitcnt lgkmcnt(0)
	v_mov_b64_e32 v[34:35], v[38:39]
	s_nop 0
	v_add_f32_e32 v34, v36, v34
	v_add_f32_e32 v34, v34, v35
	v_fmamk_f32 v34, v34, 0x3eb17218, v176
	v_lshlrev_b32 v35, 2, v0
	global_store_dword v35, v34, s[22:23]

.LBB1_186:
.LBB1_187:
	s_and_saveexec_b64 s[20:21], s[4:5]
	s_cbranch_execz .LBB1_189
	ds_read2_b32 v[34:35], v180 offset1:224
	v_add_u32_e32 v36, 0x700, v180
	ds_read2_b32 v[36:37], v36 offset1:224
	s_lshl_b64 s[22:23], s[12:13], 2
	s_add_u32 s22, s10, s22
	s_waitcnt lgkmcnt(1)
	s_addc_u32 s23, s11, s23
	v_add_f32_e32 v34, 0, v34
	v_add_f32_e32 v38, v34, v35
	s_waitcnt lgkmcnt(0)
	v_mov_b64_e32 v[34:35], v[36:37]
	v_add_u32_e32 v36, 0xe00, v180
	ds_read2_b32 v[36:37], v36 offset1:224
	v_add_f32_e32 v34, v38, v34
	v_add_u32_e32 v38, 0x1500, v180
	ds_read2_b32 v[38:39], v38 offset1:224
	v_add_f32_e32 v40, v34, v35
	s_waitcnt lgkmcnt(1)
	v_mov_b64_e32 v[34:35], v[36:37]
	s_nop 0
	v_add_f32_e32 v34, v40, v34
	v_add_f32_e32 v36, v34, v35
	s_waitcnt lgkmcnt(0)
	v_mov_b64_e32 v[34:35], v[38:39]
	s_nop 0
	v_add_f32_e32 v34, v36, v34
	v_add_f32_e32 v34, v34, v35
	v_fmamk_f32 v34, v34, 0x3eb17218, v176
	v_lshlrev_b32 v35, 2, v0
	global_store_dword v35, v34, s[22:23]

.LBB1_195:
.LBB1_196:
	s_and_saveexec_b64 s[20:21], s[4:5]
	s_cbranch_execz .LBB1_198
	ds_read2_b32 v[34:35], v216 offset1:224
	v_add_u32_e32 v36, 0x700, v216
	ds_read2_b32 v[36:37], v36 offset1:224
	s_lshl_b64 s[22:23], s[12:13], 2
	s_add_u32 s22, s10, s22
	s_waitcnt lgkmcnt(1)
	s_addc_u32 s23, s11, s23
	v_add_f32_e32 v34, 0, v34
	v_add_f32_e32 v38, v34, v35
	s_waitcnt lgkmcnt(0)
	v_mov_b64_e32 v[34:35], v[36:37]
	v_add_u32_e32 v36, 0xe00, v216
	ds_read2_b32 v[36:37], v36 offset1:224
	v_add_f32_e32 v34, v38, v34
	v_add_u32_e32 v38, 0x1500, v216
	ds_read2_b32 v[38:39], v38 offset1:224
	v_add_f32_e32 v40, v34, v35
	s_waitcnt lgkmcnt(1)
	v_mov_b64_e32 v[34:35], v[36:37]
	s_nop 0
	v_add_f32_e32 v34, v40, v34
	v_add_f32_e32 v36, v34, v35
	s_waitcnt lgkmcnt(0)
	v_mov_b64_e32 v[34:35], v[38:39]
	s_nop 0
	v_add_f32_e32 v34, v36, v34
	v_add_f32_e32 v34, v34, v35
	v_fmamk_f32 v34, v34, 0x3eb17218, v176
	v_lshlrev_b32 v35, 2, v0
	global_store_dword v35, v34, s[22:23]

.LBB1_212:
.LBB1_213:
	s_and_saveexec_b64 s[20:21], s[4:5]
	s_cbranch_execz .LBB1_215
	ds_read2_b32 v[18:19], v200 offset1:224
	v_add_u32_e32 v20, 0x700, v200
	ds_read2_b32 v[20:21], v20 offset1:224
	s_lshl_b64 s[22:23], s[12:13], 2
	s_add_u32 s22, s10, s22
	s_waitcnt lgkmcnt(1)
	s_addc_u32 s23, s11, s23
	v_add_f32_e32 v18, 0, v18
	v_add_f32_e32 v22, v18, v19
	s_waitcnt lgkmcnt(0)
	v_mov_b64_e32 v[18:19], v[20:21]
	v_add_u32_e32 v20, 0xe00, v200
	ds_read2_b32 v[20:21], v20 offset1:224
	v_add_f32_e32 v18, v22, v18
	v_add_u32_e32 v22, 0x1500, v200
	ds_read2_b32 v[22:23], v22 offset1:224
	v_add_f32_e32 v24, v18, v19
	s_waitcnt lgkmcnt(1)
	v_mov_b64_e32 v[18:19], v[20:21]
	s_nop 0
	v_add_f32_e32 v18, v24, v18
	v_add_f32_e32 v20, v18, v19
	s_waitcnt lgkmcnt(0)
	v_mov_b64_e32 v[18:19], v[22:23]
	s_nop 0
	v_add_f32_e32 v18, v20, v18
	v_add_f32_e32 v18, v18, v19
	v_fmamk_f32 v18, v18, 0x3eb17218, v176
	v_lshlrev_b32 v19, 2, v0
	global_store_dword v19, v18, s[22:23]

.LBB1_221:
.LBB1_222:
	s_and_saveexec_b64 s[20:21], s[4:5]
	s_cbranch_execz .LBB1_224
	ds_read2_b32 v[18:19], v190 offset1:224
	v_add_u32_e32 v20, 0x700, v190
	ds_read2_b32 v[20:21], v20 offset1:224
	s_lshl_b64 s[22:23], s[12:13], 2
	s_add_u32 s22, s10, s22
	s_waitcnt lgkmcnt(1)
	s_addc_u32 s23, s11, s23
	v_add_f32_e32 v18, 0, v18
	v_add_f32_e32 v22, v18, v19
	s_waitcnt lgkmcnt(0)
	v_mov_b64_e32 v[18:19], v[20:21]
	v_add_u32_e32 v20, 0xe00, v190
	ds_read2_b32 v[20:21], v20 offset1:224
	v_add_f32_e32 v18, v22, v18
	v_add_u32_e32 v22, 0x1500, v190
	ds_read2_b32 v[22:23], v22 offset1:224
	v_add_f32_e32 v24, v18, v19
	s_waitcnt lgkmcnt(1)
	v_mov_b64_e32 v[18:19], v[20:21]
	s_nop 0
	v_add_f32_e32 v18, v24, v18
	v_add_f32_e32 v20, v18, v19
	s_waitcnt lgkmcnt(0)
	v_mov_b64_e32 v[18:19], v[22:23]
	s_nop 0
	v_add_f32_e32 v18, v20, v18
	v_add_f32_e32 v18, v18, v19
	v_fmamk_f32 v18, v18, 0x3eb17218, v176
	v_lshlrev_b32 v19, 2, v0
	global_store_dword v19, v18, s[22:23]

.LBB1_237:
.LBB1_238:
	s_and_saveexec_b64 s[0:1], s[4:5]
	s_cbranch_execz .LBB1_240
	ds_read2_b32 v[2:3], v180 offset1:224
	v_add_u32_e32 v1, 0x700, v180
	ds_read2_b32 v[4:5], v1 offset1:224
	s_sub_i32 s2, 0x78, s30
	s_mul_i32 s2, s2, 6
	s_waitcnt lgkmcnt(1)
	s_ashr_i32 s3, s2, 31
	v_add_f32_e32 v1, 0, v2
	v_add_f32_e32 v1, v1, v3
	s_waitcnt lgkmcnt(0)
	v_mov_b64_e32 v[2:3], v[4:5]
	v_add_u32_e32 v4, 0xe00, v180
	ds_read2_b32 v[4:5], v4 offset1:224
	v_add_f32_e32 v1, v1, v2
	v_add_u32_e32 v2, 0x1500, v180
	ds_read2_b32 v[6:7], v2 offset1:224
	v_add_f32_e32 v1, v1, v3
	s_waitcnt lgkmcnt(1)
	v_mov_b64_e32 v[2:3], v[4:5]
	s_lshl_b64 s[4:5], s[12:13], 2
	v_add_f32_e32 v1, v1, v2
	v_add_f32_e32 v1, v1, v3
	s_waitcnt lgkmcnt(0)
	v_mov_b64_e32 v[2:3], v[6:7]
	s_add_u32 s4, s10, s4
	v_add_f32_e32 v1, v1, v2
	s_addc_u32 s5, s11, s5
	s_lshl_b64 s[2:3], s[2:3], 2
	v_add_f32_e32 v1, v1, v3
	s_add_u32 s2, s4, s2
	v_fmamk_f32 v1, v1, 0x3eb17218, v176
	s_addc_u32 s3, s5, s3
	v_lshlrev_b32 v2, 2, v0
	global_store_dword v2, v1, s[2:3]
